# baseline (speedup 1.0000x reference)
.Lk2_noprio:
	s_nop 0
	s_nop 0
